# LN1 / LN2 row loops: the wait at the top of each row no longer waits for the previous row's four stores (vmcnt(4)); first-iteration and re-load paths keep a full wait
# baseline (speedup 1.0000x reference)
; #define GAS __attribute__((address_space(1)))
; __device__ __forceinline__ void unpack8(const u32x4 q, float* o) { o[0] = bflo(q.x); o[1] = bfhi(q.x); o[2] = bflo(q.y); o[3] = bfhi(q.y); o[4] = bflo(q.z); o[5] = bfhi(q.z); o[6] = bflo(q.w); o[7] = bfhi(q.w); }
; __device__ __forceinline__ const float* mod_ptr(const Frame& F, int l, int row) { return (const float*)(F.ws + WS_MOD) + ((size_t)l * 17 + row_b(row)) * 6144; }
; __device__ __forceinline__ void ph_ln1(Frame& F, int l, int ntok) {
;     ...
;     for (int row = gw; row < ntok; row += NGW) {
;         bf16_t* xr = (bf16_t*)(F.ws + WS_XR) + (size_t)row * DM;
;         const unsigned char* yr = (const unsigned char*)(F.ws + WS_Y) + (size_t)row * DM + 16 * F.lane;
;         const float* md = mod_ptr(F, l, row);
;         const u32x4 xa = __builtin_nontemporal_load((const GAS u32x4*)(xr + cA)), xb = __builtin_nontemporal_load((const GAS u32x4*)(xr + cA + 128)), ya = __builtin_nontemporal_load((const GAS u32x4*)yr);
;         float x[16], y[16], v[16]; unpack8(xa, x); unpack8(xb, x + 8);
;         { const unsigned a[4] = {ya.x, ya.y, ya.z, ya.w};
; #pragma unroll
;           for (int e = 0; e < 4; ++e) { const f32x2 lo = __builtin_amdgcn_cvt_pk_f32_fp8((int)a[e], false), hi = __builtin_amdgcn_cvt_pk_f32_fp8((int)a[e], true); y[4 * e] = lo.x; y[4 * e + 1] = lo.y; y[4 * e + 2] = hi.x; y[4 * e + 3] = hi.y; } }
;         float s = 0.f;
; #pragma unroll
;         for (int j = 0; j < 4; ++j) { const f32x4 g1 = *(const GAS f32x4*)(md + 2048 + LN1_COL(j));
.LBB0_775:
	s_min_i32 s0, s40, 0x10000
	s_ashr_i32 s0, s0, 12
	s_ashr_i32 s2, s0, 31
	s_mul_i32 s3, s30, 17
	s_add_u32 s0, s0, s3
	s_addc_u32 s2, s2, 0
	s_mulk_i32 s2, 0x6000
	s_mul_hi_u32 s3, s0, 0x6000
	s_add_i32 s3, s3, s2
	v_lshl_add_u64 v[2:3], s[38:39], 0, v[62:63]
	s_brev_b32 s2, 38
	v_add_co_u32_e32 v68, vcc, s2, v2
	v_lshl_add_u64 v[0:1], s[38:39], 0, v[64:65]
	s_nop 0
	v_addc_co_u32_e32 v69, vcc, 0, v3, vcc
	s_nop 0
	s_mulk_i32 s0, 0x6000
	s_add_u32 s0, s22, s0
	s_addc_u32 s4, s42, s3
	s_add_u32 s2, s0, 0x2000
	s_addc_u32 s3, s4, 0
	s_add_u32 s36, s0, 0x3000
	s_addc_u32 s37, s4, 0
	v_lshl_add_u64 v[62:63], v[62:63], 0, s[18:19]
	v_lshl_add_u64 v[64:65], v[64:65], 0, s[10:11]
	s_cmp_eq_u32 s0, s88
	s_cbranch_scc1 .Lln1_md_keep
	s_mov_b32 s88, s0
	s_add_u32 s90, s0, 0x4000
	s_addc_u32 s91, s4, 0
	v_lshl_add_u64 v[236:237], s[2:3], 0, v[54:55]
	v_lshl_add_u64 v[238:239], s[2:3], 0, v[66:67]
	v_lshl_add_u64 v[240:241], s[36:37], 0, v[54:55]
	v_lshl_add_u64 v[242:243], s[36:37], 0, v[66:67]
	v_lshl_add_u64 v[244:245], s[90:91], 0, v[54:55]
	v_lshl_add_u64 v[246:247], s[90:91], 0, v[66:67]
	global_load_dwordx4 v[136:139], v[236:237], off
	global_load_dwordx4 v[140:143], v[236:237], off offset:16
	global_load_dwordx4 v[152:155], v[238:239], off
	global_load_dwordx4 v[188:191], v[238:239], off offset:16
	global_load_dwordx4 v[194:197], v[240:241], off offset:16
	global_load_dwordx4 v[198:201], v[240:241], off
	global_load_dwordx4 v[202:205], v[244:245], off offset:16
	global_load_dwordx4 v[206:209], v[244:245], off
	global_load_dwordx4 v[210:213], v[242:243], off offset:16
	global_load_dwordx4 v[214:217], v[242:243], off
	global_load_dwordx4 v[218:221], v[246:247], off offset:16
	global_load_dwordx4 v[222:225], v[246:247], off
	s_waitcnt vmcnt(0)
.Lln1_md_keep:
	s_waitcnt vmcnt(4)
	v_mov_b32_e32 v46, v128
	v_mov_b32_e32 v47, v129
	v_mov_b32_e32 v48, v130
	v_mov_b32_e32 v49, v131
	v_mov_b32_e32 v90, v132
	v_mov_b32_e32 v91, v133
	v_mov_b32_e32 v92, v134
	v_mov_b32_e32 v93, v135
	v_mov_b32_e32 v0, v144
	v_mov_b32_e32 v1, v145
	v_mov_b32_e32 v2, v146
	v_mov_b32_e32 v3, v147
	s_add_i32 s87, s40, s8
	s_cmp_lt_i32 s87, s80
	s_cselect_b64 s[86:87], -1, 0
	v_lshl_add_u64 v[148:149], s[38:39], 0, v[62:63]
	v_lshl_add_u64 v[148:149], v[148:149], 0, s[84:85]
	v_lshl_add_u64 v[150:151], s[38:39], 0, v[64:65]
	v_cndmask_b32_e64 v148, v68, v148, s[86:87]
	v_cndmask_b32_e64 v149, v69, v149, s[86:87]
	v_cndmask_b32_e64 v150, v68, v150, s[86:87]
	v_cndmask_b32_e64 v151, v69, v151, s[86:87]
	global_load_dwordx4 v[128:131], v[148:149], off nt
	global_load_dwordx4 v[132:135], v[148:149], off offset:256 nt
	global_load_dwordx4 v[144:147], v[150:151], off nt
	v_lshlrev_b32_e32 v122, 16, v93
	v_cvt_pk_f32_fp8_e32 v[24:25], v0
	v_cvt_pk_f32_fp8_sdwa v[70:71], v0 src0_sel:WORD_1
	v_cvt_pk_f32_fp8_e32 v[72:73], v1
	v_cvt_pk_f32_fp8_sdwa v[74:75], v1 src0_sel:WORD_1
	v_lshl_add_u64 v[0:1], s[2:3], 0, v[54:55]
	v_mov_b32_e32 v50, v136
	v_mov_b32_e32 v51, v137
	v_mov_b32_e32 v52, v138
	v_mov_b32_e32 v53, v139
	v_mov_b32_e32 v94, v140
	v_mov_b32_e32 v95, v141
	v_mov_b32_e32 v96, v142
	v_mov_b32_e32 v97, v143
	v_lshl_add_u64 v[0:1], s[2:3], 0, v[66:67]
	v_mov_b32_e32 v98, v152
	v_mov_b32_e32 v99, v153
	v_mov_b32_e32 v100, v154
	v_mov_b32_e32 v101, v155
	v_mov_b32_e32 v102, v188
	v_mov_b32_e32 v103, v189
	v_mov_b32_e32 v104, v190
	v_mov_b32_e32 v105, v191
	s_add_u32 s2, s0, 0x4000
	s_addc_u32 s3, s4, 0
	v_lshl_add_u64 v[0:1], s[36:37], 0, v[54:55]
	v_lshl_add_u64 v[4:5], s[2:3], 0, v[54:55]
	v_cvt_pk_f32_fp8_e32 v[114:115], v2
	v_cvt_pk_f32_fp8_sdwa v[116:117], v2 src0_sel:WORD_1
	v_cvt_pk_f32_fp8_e32 v[118:119], v3
	v_cvt_pk_f32_fp8_sdwa v[120:121], v3 src0_sel:WORD_1
	v_mov_b32_e32 v26, v156
	v_mov_b32_e32 v27, v157
	v_mov_b32_e32 v28, v158
	v_mov_b32_e32 v29, v159
	v_mov_b32_e32 v106, v160
	v_mov_b32_e32 v107, v161
	v_mov_b32_e32 v108, v162
	v_mov_b32_e32 v109, v163
	v_mov_b32_e32 v30, v164
	v_mov_b32_e32 v31, v165
	v_mov_b32_e32 v32, v166
	v_mov_b32_e32 v33, v167
	v_mov_b32_e32 v110, v168
	v_mov_b32_e32 v111, v169
	v_mov_b32_e32 v112, v170
	v_mov_b32_e32 v113, v171
	v_mov_b32_e32 v12, v194
	v_mov_b32_e32 v13, v195
	v_mov_b32_e32 v14, v196
	v_mov_b32_e32 v15, v197
	v_mov_b32_e32 v42, v198
	v_mov_b32_e32 v43, v199
	v_mov_b32_e32 v44, v200
	v_mov_b32_e32 v45, v201
	s_nop 0
	v_mov_b32_e32 v0, v202
	v_mov_b32_e32 v1, v203
	v_mov_b32_e32 v2, v204
	v_mov_b32_e32 v3, v205
	s_nop 0
	v_mov_b32_e32 v4, v206
	v_mov_b32_e32 v5, v207
	v_mov_b32_e32 v6, v208
	v_mov_b32_e32 v7, v209
	v_and_b32_e32 v123, 0xffff0000, v93
	v_lshl_add_u64 v[82:83], s[2:3], 0, v[66:67]
	s_waitcnt lgkmcnt(0)
; #define GAS __attribute__((address_space(1)))
; __device__ __forceinline__ void ph_ln1(Frame& F, int l, int ntok) {
;     ...
;         for (int j = 0; j < 4; ++j) { const f32x4 g1 = *(const GAS f32x4*)(md + 2048 + LN1_COL(j));
; #pragma unroll
;             for (int e = 0; e < 4; ++e) { v[4 * j + e] = x[4 * j + e] * DN_ALPHA + g1[e] * y[4 * j + e]; s += v[4 * j + e]; } }
;         const float mean = wave_sum(s, F.lane) * (1.f / DM); float s2 = 0.f;
; #pragma unroll
;         for (int e = 0; e < 16; ++e) { v[e] -= mean; s2 += v[e] * v[e]; }
;         const float rstd = 1.f / sqrtf(wave_sum(s2, F.lane) * (1.f / DM) + LN_EPS);
;         unsigned wx[8]; int w8[4];
; #pragma unroll
;         for (int j = 0; j < 4; ++j) { const f32x4 g = *(const GAS f32x4*)(lg + LN1_COL(j)), bb = *(const GAS f32x4*)(lb + LN1_COL(j)), sh = *(const GAS f32x4*)(md + 3072 + LN1_COL(j)), sc = *(const GAS f32x4*)(md + 4096 + LN1_COL(j));
	v_mov_b32_e32 v8, v172
	v_mov_b32_e32 v9, v173
	v_mov_b32_e32 v10, v174
	v_mov_b32_e32 v11, v175
	v_mov_b32_e32 v34, v176
	v_mov_b32_e32 v35, v177
	v_mov_b32_e32 v36, v178
	v_mov_b32_e32 v37, v179
	v_mov_b32_e32 v16, v180
	v_mov_b32_e32 v17, v181
	v_mov_b32_e32 v18, v182
	v_mov_b32_e32 v19, v183
	v_mov_b32_e32 v38, v184
	v_mov_b32_e32 v39, v185
	v_mov_b32_e32 v40, v186
	v_mov_b32_e32 v41, v187
	s_mov_b32 s0, 0x5be00000
	s_add_i32 s40, s40, s8
	s_cmp_lt_i32 s40, s80
	v_pk_mul_f32 v[52:53], v[70:71], v[52:53]
	v_lshlrev_b32_e32 v70, 16, v46
	v_and_b32_e32 v71, 0xffff0000, v46
	v_pk_mul_f32 v[24:25], v[24:25], v[50:51]
	v_pk_mul_f32 v[104:105], v[120:121], v[104:105]
	v_lshlrev_b32_e32 v120, 16, v92
	v_and_b32_e32 v121, 0xffff0000, v92
	v_pk_mul_f32 v[92:93], v[118:119], v[102:103]
	v_lshlrev_b32_e32 v102, 16, v91
	v_and_b32_e32 v103, 0xffff0000, v91
	v_pk_mul_f32 v[100:101], v[116:117], v[100:101]
	v_pk_fma_f32 v[24:25], v[70:71], s[20:21], v[24:25] op_sel_hi:[1,0,1]
	v_pk_fma_f32 v[100:101], v[102:103], s[20:21], v[100:101] op_sel_hi:[1,0,1]
	v_lshlrev_b32_e32 v102, 16, v90
	v_and_b32_e32 v103, 0xffff0000, v90
	v_pk_mul_f32 v[90:91], v[114:115], v[98:99]
	v_lshlrev_b32_e32 v98, 16, v49
	v_and_b32_e32 v99, 0xffff0000, v49
	v_pk_mul_f32 v[74:75], v[74:75], v[96:97]
	v_lshlrev_b32_e32 v96, 16, v48
	v_and_b32_e32 v97, 0xffff0000, v48
	v_pk_mul_f32 v[48:49], v[72:73], v[94:95]
	v_lshlrev_b32_e32 v72, 16, v47
	v_and_b32_e32 v73, 0xffff0000, v47
	v_add_f32_e32 v46, 0, v24
	v_pk_fma_f32 v[52:53], v[72:73], s[20:21], v[52:53] op_sel_hi:[1,0,1]
	v_add_f32_e32 v46, v25, v46
	v_add_f32_e32 v46, v52, v46
	v_pk_fma_f32 v[48:49], v[96:97], s[20:21], v[48:49] op_sel_hi:[1,0,1]
	v_add_f32_e32 v46, v53, v46
	v_add_f32_e32 v46, v48, v46
	v_pk_fma_f32 v[74:75], v[98:99], s[20:21], v[74:75] op_sel_hi:[1,0,1]
	v_add_f32_e32 v46, v49, v46
	v_add_f32_e32 v46, v74, v46
	v_pk_fma_f32 v[90:91], v[102:103], s[20:21], v[90:91] op_sel_hi:[1,0,1]
	v_add_f32_e32 v46, v75, v46
	v_add_f32_e32 v46, v90, v46
	v_add_f32_e32 v46, v91, v46
	v_add_f32_e32 v46, v100, v46
	v_pk_fma_f32 v[92:93], v[120:121], s[20:21], v[92:93] op_sel_hi:[1,0,1]
	v_add_f32_e32 v46, v101, v46
	v_add_f32_e32 v46, v92, v46
	v_pk_fma_f32 v[104:105], v[122:123], s[20:21], v[104:105] op_sel_hi:[1,0,1]
	v_add_f32_e32 v46, v93, v46
	v_add_f32_e32 v46, v104, v46
	v_add_f32_e32 v46, v105, v46
	ds_bpermute_b32 v47, v76, v46
	v_add_f32_e32 v124, 1.0, v4
	v_add_f32_e32 v125, 1.0, v5
	v_lshl_add_u64 v[4:5], s[36:37], 0, v[66:67]
	v_add_f32_e32 v126, 1.0, v6
	s_waitcnt lgkmcnt(0)
	v_add_f32_e32 v46, v46, v47
	ds_bpermute_b32 v47, v77, v46
	v_add_f32_e32 v127, 1.0, v7
	v_add_f32_e32 v86, 1.0, v0
	v_add_f32_e32 v87, 1.0, v1
	v_add_f32_e32 v88, 1.0, v2
	s_waitcnt lgkmcnt(0)
	v_add_f32_e32 v46, v46, v47
	ds_bpermute_b32 v47, v78, v46
	v_add_f32_e32 v89, 1.0, v3
	v_mov_b32_e32 v0, v210
	v_mov_b32_e32 v1, v211
	v_mov_b32_e32 v2, v212
	v_mov_b32_e32 v3, v213
	v_mov_b32_e32 v20, v214
	v_mov_b32_e32 v21, v215
	v_mov_b32_e32 v22, v216
	v_mov_b32_e32 v23, v217
	s_nop 0
	v_mov_b32_e32 v4, v218
	v_mov_b32_e32 v5, v219
	v_mov_b32_e32 v6, v220
	v_mov_b32_e32 v7, v221
	s_nop 0
	v_mov_b32_e32 v82, v222
	v_mov_b32_e32 v83, v223
	v_mov_b32_e32 v84, v224
	v_mov_b32_e32 v85, v225
	s_cselect_b32 s89, 1, 0
	s_min_i32 s86, s40, 0x10000
	s_ashr_i32 s86, s86, 12
	s_mul_i32 s87, s30, 17
	s_add_i32 s86, s86, s87
	s_mul_hi_u32 s87, s86, 0x6000
	s_mul_i32 s86, s86, 0x6000
	s_add_u32 s86, s22, s86
	s_addc_u32 s87, s42, s87
	s_cmp_eq_u32 s86, s88
	s_cbranch_scc1 .Lln1_md_next_keep
	s_mov_b32 s88, s86
	s_add_u32 s90, s86, 0x2000
	s_addc_u32 s91, s87, 0
	v_lshl_add_u64 v[236:237], s[90:91], 0, v[54:55]
	s_add_u32 s90, s86, 0x2000
	s_addc_u32 s91, s87, 0
	v_lshl_add_u64 v[238:239], s[90:91], 0, v[66:67]
	s_add_u32 s90, s86, 0x3000
	s_addc_u32 s91, s87, 0
	v_lshl_add_u64 v[240:241], s[90:91], 0, v[54:55]
	s_add_u32 s90, s86, 0x3000
	s_addc_u32 s91, s87, 0
	v_lshl_add_u64 v[242:243], s[90:91], 0, v[66:67]
	s_add_u32 s90, s86, 0x4000
	s_addc_u32 s91, s87, 0
	v_lshl_add_u64 v[244:245], s[90:91], 0, v[54:55]
	s_add_u32 s90, s86, 0x4000
	s_addc_u32 s91, s87, 0
	v_lshl_add_u64 v[246:247], s[90:91], 0, v[66:67]
	global_load_dwordx4 v[136:139], v[236:237], off
	global_load_dwordx4 v[140:143], v[236:237], off offset:16
	global_load_dwordx4 v[152:155], v[238:239], off
	global_load_dwordx4 v[188:191], v[238:239], off offset:16
	global_load_dwordx4 v[194:197], v[240:241], off offset:16
	global_load_dwordx4 v[198:201], v[240:241], off
	global_load_dwordx4 v[202:205], v[244:245], off offset:16
	global_load_dwordx4 v[206:209], v[244:245], off
	global_load_dwordx4 v[210:213], v[242:243], off offset:16
	global_load_dwordx4 v[214:217], v[242:243], off
	global_load_dwordx4 v[218:221], v[246:247], off offset:16
	global_load_dwordx4 v[222:225], v[246:247], off

; #define GAS __attribute__((address_space(1)))
; __device__ __forceinline__ void ph_ln2(Frame& F, int l, int ntok, bool last) {
;     const int gw = F.wg * NWAVES + F.wave, NGW = F.G * NWAVES;
;     const int cA = 256 * (F.lane >> 4) + 32 * ((F.lane >> 2) & 3) + 8 * (F.lane & 3);
;     ...
;     const float* lg = F.in[I_LN2G] + l * DM; const float* lb = F.in[I_LN2B] + l * DM;
;     struct Ln2Raw { u32x2 q[8]; u32x4 qs, xa, xb; };
;     auto ln2_load = [&](int row) { Ln2Raw r;
;         const unsigned char* y2 = (const unsigned char*)(F.ws + WS_Y2) + (size_t)row * 5120;
;         const bf16_t* xr = (const bf16_t*)(F.ws + WS_XR) + (size_t)row * DM;
; #pragma unroll
;         for (int k = 0; k < 8; ++k) r.q[k] = __builtin_nontemporal_load((const GAS u32x2*)(y2 + k * 512 + 8 * F.lane));
;         r.qs = __builtin_nontemporal_load((const GAS u32x4*)(y2 + 4096 + 16 * F.lane));
;         r.xa = __builtin_nontemporal_load((const GAS u32x4*)(xr + cA)); r.xb = __builtin_nontemporal_load((const GAS u32x4*)(xr + cA + 128));
;         return r; };
;     Ln2Raw cur = ln2_load(gw < ntok ? gw : 0);
.LBB0_1687:
	v_readlane_b32 s36, v252, 8
	s_mov_b32 s0, s97
	v_readlane_b32 s38, v252, 10
	v_readlane_b32 s39, v252, 11
	v_readlane_b32 s4, v254, 28
	v_mbcnt_lo_u32_b32 v8, -1, 0
	v_mbcnt_hi_u32_b32 v8, -1, v8
	v_readlane_b32 s37, v252, 9
	s_mov_b64 s[20:21], s[38:39]
	s_add_i32 s38, s0, s4
	s_mov_b64 s[2:3], s[36:37]
	s_cmp_ge_i32 s38, s80
	s_cbranch_scc1 .LBB0_1696
	s_lshl_b32 s22, s30, 10
	v_readlane_b32 s40, v252, 0
	s_lshl_b64 s[4:5], s[22:23], 2
	v_readlane_b32 s46, v252, 6
	v_readlane_b32 s47, v252, 7
	s_add_u32 s18, s46, s4
	v_readlane_b32 s44, v252, 4
	s_addc_u32 s19, s47, s5
	v_readlane_b32 s45, v252, 5
	s_add_u32 s4, s44, s4
	s_addc_u32 s5, s45, s5
	s_add_u32 s36, s20, 0x64000000
	v_lshlrev_b32_e32 v34, 3, v8
	v_readlane_b32 s42, v252, 2
	v_readlane_b32 s43, v252, 3
	s_addc_u32 s37, s21, 0
	s_ashr_i32 s39, s38, 31
	v_lshlrev_b32_e32 v32, 4, v8
	v_and_b32_e32 v0, 0x78, v34
	s_movk_i32 s0, 0xff00
	s_lshl_b64 s[42:43], s[38:39], 11
	v_and_or_b32 v36, v32, s0, v0
	v_readlane_b32 s41, v252, 1
	s_add_u32 s40, s36, s42
	v_ashrrev_i32_e32 v37, 31, v36
	s_addc_u32 s41, s37, s43
	v_lshlrev_b64 v[10:11], 1, v[36:37]
	s_add_u32 s22, s20, 0x2f600000
	v_lshl_add_u64 v[0:1], s[40:41], 0, v[10:11]
	s_addc_u32 s44, s21, 0
	s_mul_i32 s40, s38, 0x1400
	s_mul_hi_i32 s0, s38, 0x1400
	s_add_u32 s40, s22, s40
	s_addc_u32 s41, s44, s0
	v_ashrrev_i32_e32 v33, 31, v32
	s_waitcnt vmcnt(0)
	v_lshl_add_u64 v[4:5], s[40:41], 0, v[32:33]
	s_movk_i32 s0, 0x1000
	v_add_co_u32_e32 v4, vcc, s0, v4
	v_ashrrev_i32_e32 v35, 31, v34
	s_nop 0
	v_addc_co_u32_e32 v5, vcc, 0, v5, vcc
	v_lshl_add_u64 v[16:17], s[40:41], 0, v[34:35]
	global_load_dwordx4 v[12:15], v[0:1], off offset:256 nt
	s_nop 0
	global_load_dwordx4 v[0:3], v[0:1], off nt
	s_nop 0
	global_load_dwordx2 v[66:67], v[16:17], off offset:3584 nt
	global_load_dwordx2 v[64:65], v[16:17], off offset:3072 nt
	global_load_dwordx2 v[62:63], v[16:17], off offset:2560 nt
	global_load_dwordx2 v[60:61], v[16:17], off offset:2048 nt
	global_load_dwordx2 v[58:59], v[16:17], off offset:1536 nt
	global_load_dwordx2 v[56:57], v[16:17], off offset:1024 nt
	global_load_dwordx2 v[54:55], v[16:17], off offset:512 nt
	s_nop 0
	global_load_dwordx4 v[4:7], v[4:5], off nt
	s_nop 0
	global_load_dwordx2 v[52:53], v[16:17], off nt
	s_mul_i32 s45, s30, 17
	s_add_i32 s46, s45, 17
	v_lshlrev_b64 v[40:41], 2, v[36:37]
	s_add_u32 s47, s20, 0x100000
	v_lshl_add_u64 v[42:43], s[4:5], 0, v[40:41]
	s_addc_u32 s48, s21, 0
	s_lshl_b64 s[40:41], s[38:39], 5
	s_lshl_b64 s[4:5], s[38:39], 12
	s_add_u32 s2, s2, s4
	v_or_b32_e32 v38, 0x80, v36
	v_lshlrev_b32_e32 v8, 2, v8
	s_addc_u32 s3, s3, s5
	v_ashrrev_i32_e32 v39, 31, v38
	v_lshl_add_u64 v[44:45], s[18:19], 0, v[40:41]
	v_lshl_add_u64 v[46:47], s[36:37], 0, v[10:11]
	v_xor_b32_e32 v103, 4, v8
	v_xor_b32_e32 v107, 8, v8
	v_xor_b32_e32 v113, 16, v8
	v_xor_b32_e32 v170, 32, v8
	v_xor_b32_e32 v171, 64, v8
	v_xor_b32_e32 v172, 0x80, v8
	v_lshl_add_u64 v[48:49], s[2:3], 0, v[40:41]
	v_lshl_add_u64 v[50:51], s[42:43], 0, v[10:11]
	global_load_dwordx4 v[182:185], v[42:43], off offset:16
	global_load_dwordx4 v[186:189], v[42:43], off
	global_load_dwordx4 v[194:197], v[44:45], off offset:16
	global_load_dwordx4 v[198:201], v[44:45], off
	global_load_dwordx4 v[202:205], v[42:43], off offset:528
	global_load_dwordx4 v[216:219], v[42:43], off offset:512
	global_load_dwordx4 v[220:223], v[44:45], off offset:528
	global_load_dwordx4 v[236:239], v[44:45], off offset:512
	s_mov_b32 s88, 1
	s_mov_b32 s89, 1
	s_waitcnt vmcnt(0)
	s_branch .LBB0_1690

; __device__ __forceinline__ const float* mod_ptr(const Frame& F, int l, int row) { return (const float*)(F.ws + WS_MOD) + ((size_t)l * 17 + row_b(row)) * 6144; }
; __device__ __forceinline__ void ph_ln2(Frame& F, int l, int ntok, bool last) {
;     ...
;     for (int row = gw; row < ntok; row += NGW) {
;         const Ln2Raw nxt = ln2_load(row + NGW < ntok ? row + NGW : row);
;         bf16_t* xr = (bf16_t*)(F.ws + WS_XR) + (size_t)row * DM;
;         const float* wg = (const float*)(F.ws + WS_WGT) + (size_t)row * 8;
;         const float* md = mod_ptr(F, l, row);
;         float ff[16];
; #pragma unroll
;         for (int e = 0; e < 16; ++e) ff[e] = 0.f;
;         { const unsigned a[4] = {cur.qs.x, cur.qs.y, cur.qs.z, cur.qs.w};
; #pragma unroll
;           for (int e = 0; e < 4; ++e) { const f32x2 lo = __builtin_amdgcn_cvt_pk_f32_fp8((int)a[e], false), hi = __builtin_amdgcn_cvt_pk_f32_fp8((int)a[e], true);
;               ff[4 * e] += pg8::Y2_INV * lo.x; ff[4 * e + 1] += pg8::Y2_INV * lo.y; ff[4 * e + 2] += pg8::Y2_INV * hi.x; ff[4 * e + 3] += pg8::Y2_INV * hi.y; } }
; #pragma unroll
;         for (int k = 0; k < 8; ++k) { const float wk = wg[k] * pg8::Y2_INV; const unsigned a[2] = {cur.q[k].x, cur.q[k].y};
; #pragma unroll
;             for (int h = 0; h < 2; ++h) {
;                 const f32x2 p0 = __builtin_amdgcn_cvt_scalef32_pk_f32_fp4(a[h], 1.0f, 0), p1 = __builtin_amdgcn_cvt_scalef32_pk_f32_fp4(a[h], 1.0f, 1), p2 = __builtin_amdgcn_cvt_scalef32_pk_f32_fp4(a[h], 1.0f, 2), p3 = __builtin_amdgcn_cvt_scalef32_pk_f32_fp4(a[h], 1.0f, 3);
;                 ff[8 * h] += wk * p0.x; ff[8 * h + 1] += wk * p0.y; ff[8 * h + 2] += wk * p1.x; ff[8 * h + 3] += wk * p1.y; ff[8 * h + 4] += wk * p2.x; ff[8 * h + 5] += wk * p2.y; ff[8 * h + 6] += wk * p3.x; ff[8 * h + 7] += wk * p3.y; } }
.LBB0_1690:
	v_readlane_b32 s2, v255, 14
	s_mov_b32 s0, s38
	s_add_i32 s38, s38, s2
	s_cmp_ge_i32 s38, s80
	s_cselect_b64 s[42:43], -1, 0
	s_cmp_lt_i32 s38, s80
	v_readlane_b32 s3, v255, 15
	s_cselect_b32 s2, s38, s0
	s_ashr_i32 s3, s2, 31
	s_mul_i32 s4, s2, 0x1400
	s_mul_hi_i32 s5, s2, 0x1400
	s_add_u32 s4, s22, s4
	s_waitcnt vmcnt(4)
	v_mov_b64_e32 v[18:19], v[2:3]
	s_addc_u32 s5, s44, s5
	v_mov_b64_e32 v[16:17], v[0:1]
	v_lshl_add_u64 v[0:1], s[4:5], 0, v[34:35]
	v_mov_b64_e32 v[20:21], v[66:67]
	v_mov_b64_e32 v[22:23], v[64:65]
	v_mov_b64_e32 v[24:25], v[62:63]
	v_mov_b64_e32 v[26:27], v[60:61]
	v_mov_b64_e32 v[70:71], v[58:59]
	v_mov_b64_e32 v[28:29], v[56:57]
	v_mov_b64_e32 v[30:31], v[54:55]
	v_mov_b64_e32 v[68:69], v[52:53]
	global_load_dwordx2 v[52:53], v[0:1], off nt
	global_load_dwordx2 v[54:55], v[0:1], off offset:512 nt
	global_load_dwordx2 v[56:57], v[0:1], off offset:1024 nt
	global_load_dwordx2 v[58:59], v[0:1], off offset:1536 nt
	global_load_dwordx2 v[60:61], v[0:1], off offset:2048 nt
	global_load_dwordx2 v[62:63], v[0:1], off offset:2560 nt
	global_load_dwordx2 v[64:65], v[0:1], off offset:3072 nt
	global_load_dwordx2 v[66:67], v[0:1], off offset:3584 nt
	s_lshl_b64 s[2:3], s[2:3], 11
	v_lshl_add_u64 v[0:1], s[4:5], 0, v[32:33]
	s_movk_i32 s4, 0x1000
	v_add_co_u32_e32 v0, vcc, s4, v0
	s_add_u32 s4, s20, s40
	s_addc_u32 s5, s21, s41
	s_min_i32 s0, s0, 0x10000
	s_ashr_i32 s39, s0, 12
	s_ashr_i32 s49, s39, 31
	s_waitcnt lgkmcnt(0)
	v_lshl_add_u64 v[8:9], v[46:47], 0, s[2:3]
	s_add_u32 s2, s39, s45
	v_mov_b64_e32 v[74:75], v[6:7]
	s_addc_u32 s0, s49, 0
	v_mov_b64_e32 v[72:73], v[4:5]
	s_mulk_i32 s0, 0x6000
	s_mul_hi_u32 s3, s2, 0x6000
	v_addc_co_u32_e32 v1, vcc, 0, v1, vcc
	s_add_i32 s3, s3, s0
	v_cvt_pk_f32_fp8_e32 v[76:77], v72
	v_cvt_pk_f32_fp8_sdwa v[78:79], v72 src0_sel:WORD_1
	v_mov_b32_e32 v72, s4
	s_mov_b32 s0, 0x1a600000
	v_add_co_u32_e32 v98, vcc, s0, v72
	v_mov_b32_e32 v72, s5
	s_nop 0
	v_addc_co_u32_e32 v99, vcc, 0, v72, vcc
	global_load_dwordx4 v[4:7], v[0:1], off nt
	s_nop 0
	global_load_dwordx4 v[0:3], v[8:9], off nt
	s_nop 0
	global_load_dwordx4 v[8:11], v[8:9], off offset:256 nt
	v_cvt_pk_f32_fp8_e32 v[80:81], v73
	v_cvt_pk_f32_fp8_sdwa v[84:85], v73 src0_sel:WORD_1
	v_cvt_pk_f32_fp8_e32 v[88:89], v74
	v_cvt_pk_f32_fp8_sdwa v[92:93], v74 src0_sel:WORD_1
	v_cvt_pk_f32_fp8_e32 v[94:95], v75
	v_cvt_pk_f32_fp8_sdwa v[96:97], v75 src0_sel:WORD_1
	flat_load_dwordx4 v[72:75], v[98:99]
	s_mov_b32 s0, 0x3e000000
	v_cvt_scalef32_pk_f32_fp4 v[82:83], v68, 1.0
	v_pk_fma_f32 v[76:77], v[76:77], s[0:1], 0 op_sel_hi:[1,0,0]
	v_cvt_scalef32_pk_f32_fp4 v[86:87], v68, 1.0 op_sel:[1,0,0]
	v_cvt_scalef32_pk_f32_fp4 v[104:105], v68, 1.0 op_sel:[0,1,0]
	v_cvt_scalef32_pk_f32_fp4 v[108:109], v68, 1.0 op_sel:[1,1,0]
	v_cvt_scalef32_pk_f32_fp4 v[110:111], v69, 1.0
	v_cvt_scalef32_pk_f32_fp4 v[114:115], v69, 1.0 op_sel:[1,0,0]
	v_cvt_scalef32_pk_f32_fp4 v[116:117], v69, 1.0 op_sel:[0,1,0]
	v_cvt_scalef32_pk_f32_fp4 v[118:119], v69, 1.0 op_sel:[1,1,0]
	v_cvt_scalef32_pk_f32_fp4 v[68:69], v30, 1.0
	v_cvt_scalef32_pk_f32_fp4 v[90:91], v28, 1.0
	v_cvt_scalef32_pk_f32_fp4 v[130:131], v28, 1.0 op_sel:[1,0,0]
	v_cvt_scalef32_pk_f32_fp4 v[120:121], v30, 1.0 op_sel:[0,1,0]
	v_cvt_scalef32_pk_f32_fp4 v[132:133], v28, 1.0 op_sel:[0,1,0]
	v_cvt_scalef32_pk_f32_fp4 v[122:123], v30, 1.0 op_sel:[1,1,0]
	v_cvt_scalef32_pk_f32_fp4 v[124:125], v31, 1.0
	v_cvt_scalef32_pk_f32_fp4 v[134:135], v28, 1.0 op_sel:[1,1,0]
	v_cvt_scalef32_pk_f32_fp4 v[126:127], v31, 1.0 op_sel:[1,0,0]
	s_mulk_i32 s2, 0x6000
	v_cvt_scalef32_pk_f32_fp4 v[128:129], v31, 1.0 op_sel:[0,1,0]
	s_add_u32 s2, s47, s2
	s_addc_u32 s3, s48, s3
	s_add_u32 s36, s2, 0x5000
	s_addc_u32 s37, s3, 0
	s_cmp_eq_u32 s36, s89
	s_cbranch_scc1 .Lln2_g2_keep
	s_mov_b32 s89, s36
	v_lshl_add_u64 v[248:249], v[36:37], 2, s[36:37]
	v_lshl_add_u64 v[250:251], v[38:39], 2, s[36:37]
	global_load_dwordx4 v[206:209], v[248:249], off offset:16
	global_load_dwordx4 v[210:213], v[248:249], off
	global_load_dwordx4 v[240:243], v[250:251], off offset:16
	global_load_dwordx4 v[244:247], v[250:251], off
